# adds: prologue adaLN projection on the f32 matrix cores (v_mfma_f32_32x32x2_f32) instead of broadcast-LDS packed f32 FMAs
# speedup vs baseline: 1.0093x; 1.0038x over previous
.LBB0_63:
	s_or_b64 exec, exec, s[28:29]
	global_load_dword v14, v[20:21], off
	v_add_u32_e32 v21, 0x200, v23
	v_cmp_lt_i32_e32 vcc, s35, v23
	v_lshl_add_u64 v[18:19], v[18:19], 0, s[20:21]
	s_or_b64 s[24:25], vcc, s[24:25]
	v_mov_b32_e32 v23, v21
	s_waitcnt vmcnt(0)
	v_mul_f32_e32 v20, 0xbfb8aa3b, v14
	v_exp_f32_e32 v20, v20
	s_nop 0
	v_add_f32_e32 v20, 1.0, v20
	v_rcp_f32_e32 v20, v20
	s_nop 0
	v_mul_f32_e32 v14, v14, v20
	v_add_u32_e32 v24, 0xfffffe00, v23
	v_lshrrev_b32_e32 v24, 10, v24
	v_lshl_add_u32 v24, v24, 4, v22
	ds_write_b32 v24, v14
	v_add_u32_e32 v22, 0x800, v22
	s_andn2_b64 exec, exec, s[24:25]
	s_cbranch_execz .LBB0_68

.LBB0_68:
	s_or_b64 exec, exec, s[0:1]
	s_mul_i32 s42, s40, 0x556
	s_lshr_b32 s42, s42, 16
	s_mul_i32 s43, s42, 48
	s_sub_i32 s43, s40, s43
	s_lshl_b32 s43, s43, 7
	s_load_dwordx2 s[44:45], s[2:3], 0x20
	s_load_dwordx2 s[46:47], s[2:3], 0x28
	v_and_b32_e32 v18, 63, v2
	v_lshrrev_b32_e32 v19, 6, v2
	v_and_b32_e32 v20, 31, v18
	v_readfirstlane_b32 s48, v19
	v_lshrrev_b32_e32 v21, 5, v18
	s_and_b32 s49, s48, 3
	s_lshr_b32 s50, s48, 2
	s_mul_i32 s51, s42, 0x1800000
	s_mul_i32 s52, s50, 0xc00000
	s_add_i32 s51, s51, s52
	s_lshl_b32 s52, s49, 7
	s_add_i32 s51, s51, s52
	s_lshl_b32 s52, s43, 2
	s_add_i32 s51, s51, s52
	v_mul_u32_u24_e32 v22, 0x18000, v21
	v_lshl_add_u32 v22, v20, 2, v22
	v_add_u32_e32 v22, s51, v22
	v_add_u32_e32 v23, 0x6000, v22
	v_add_u32_e32 v24, 0xc000, v22
	v_add_u32_e32 v25, 0x12000, v22
	v_mul_u32_u24_e32 v26, 4112, v20
	s_lshl_b32 s52, s50, 11
	v_lshl_add_u32 v26, v21, 4, v26
	v_add_u32_e32 v26, s52, v26
	v_lshlrev_b32_e32 v27, 4, v21
	v_add_u32_e32 v27, s52, v27
	v_add_u32_e32 v27, 0x20200, v27
	v_mov_b32_e32 v32, 0
	v_mov_b32_e32 v33, 0
	v_mov_b32_e32 v34, 0
	v_mov_b32_e32 v35, 0
	v_mov_b32_e32 v36, 0
	v_mov_b32_e32 v37, 0
	v_mov_b32_e32 v38, 0
	v_mov_b32_e32 v39, 0
	v_mov_b32_e32 v40, 0
	v_mov_b32_e32 v41, 0
	v_mov_b32_e32 v42, 0
	v_mov_b32_e32 v43, 0
	v_mov_b32_e32 v44, 0
	v_mov_b32_e32 v45, 0
	v_mov_b32_e32 v46, 0
	v_mov_b32_e32 v47, 0
	v_mov_b32_e32 v30, 0
	s_waitcnt lgkmcnt(0)
	s_barrier
	global_load_dword v80, v22, s[44:45]
	global_load_dword v81, v23, s[44:45]
	global_load_dword v82, v24, s[44:45]
	global_load_dword v83, v25, s[44:45]
	s_add_u32 s44, s44, 0x30000
	s_addc_u32 s45, s45, 0
	global_load_dword v84, v22, s[44:45]
	global_load_dword v85, v23, s[44:45]
	global_load_dword v86, v24, s[44:45]
	global_load_dword v87, v25, s[44:45]
	s_add_u32 s44, s44, 0x30000
	s_addc_u32 s45, s45, 0
	global_load_dword v88, v22, s[44:45]
	global_load_dword v89, v23, s[44:45]
	global_load_dword v90, v24, s[44:45]
	global_load_dword v91, v25, s[44:45]
	s_add_u32 s44, s44, 0x30000
	s_addc_u32 s45, s45, 0
	global_load_dword v92, v22, s[44:45]
	global_load_dword v93, v23, s[44:45]
	global_load_dword v94, v24, s[44:45]
	global_load_dword v95, v25, s[44:45]
	s_add_u32 s44, s44, 0x30000
	s_addc_u32 s45, s45, 0
	global_load_dword v108, v22, s[44:45]
	global_load_dword v109, v23, s[44:45]
	global_load_dword v110, v24, s[44:45]
	global_load_dword v111, v25, s[44:45]
	s_add_u32 s44, s44, 0x30000
	s_addc_u32 s45, s45, 0
	global_load_dword v112, v22, s[44:45]
	global_load_dword v113, v23, s[44:45]
	global_load_dword v114, v24, s[44:45]
	global_load_dword v115, v25, s[44:45]
	s_add_u32 s44, s44, 0x30000
	s_addc_u32 s45, s45, 0
	global_load_dword v116, v22, s[44:45]
	global_load_dword v117, v23, s[44:45]
	global_load_dword v118, v24, s[44:45]
	global_load_dword v119, v25, s[44:45]
	s_add_u32 s44, s44, 0x30000
	s_addc_u32 s45, s45, 0
	global_load_dword v120, v22, s[44:45]
	global_load_dword v121, v23, s[44:45]
	global_load_dword v122, v24, s[44:45]
	global_load_dword v123, v25, s[44:45]
	s_add_u32 s44, s44, 0x30000
	s_addc_u32 s45, s45, 0
	global_load_dword v124, v22, s[44:45]
	global_load_dword v125, v23, s[44:45]
	global_load_dword v126, v24, s[44:45]
	global_load_dword v127, v25, s[44:45]
	s_add_u32 s44, s44, 0x30000
	s_addc_u32 s45, s45, 0
	global_load_dword v128, v22, s[44:45]
	global_load_dword v129, v23, s[44:45]
	global_load_dword v130, v24, s[44:45]
	global_load_dword v131, v25, s[44:45]
	s_add_u32 s44, s44, 0x30000
	s_addc_u32 s45, s45, 0
	global_load_dword v132, v22, s[44:45]
	global_load_dword v133, v23, s[44:45]
	global_load_dword v134, v24, s[44:45]
	global_load_dword v135, v25, s[44:45]
	s_add_u32 s44, s44, 0x30000
	s_addc_u32 s45, s45, 0
	global_load_dword v136, v22, s[44:45]
	global_load_dword v137, v23, s[44:45]
	global_load_dword v138, v24, s[44:45]
	global_load_dword v139, v25, s[44:45]
	s_add_u32 s44, s44, 0x30000
	s_addc_u32 s45, s45, 0
	ds_read_b128 v[64:67], v26 offset:0
	ds_read_b128 v[72:75], v27 offset:0
	global_load_dword v48, v22, s[44:45]
	global_load_dword v49, v23, s[44:45]
	global_load_dword v50, v24, s[44:45]
	global_load_dword v51, v25, s[44:45]
	s_add_u32 s44, s44, 0x30000
	s_addc_u32 s45, s45, 0
	global_load_dword v52, v22, s[44:45]
	global_load_dword v53, v23, s[44:45]
	global_load_dword v54, v24, s[44:45]
	global_load_dword v55, v25, s[44:45]
	s_add_u32 s44, s44, 0x30000
	s_addc_u32 s45, s45, 0
	global_load_dword v56, v22, s[44:45]
	global_load_dword v57, v23, s[44:45]
	global_load_dword v58, v24, s[44:45]
	global_load_dword v59, v25, s[44:45]
	s_add_u32 s44, s44, 0x30000
	s_addc_u32 s45, s45, 0
	global_load_dword v60, v22, s[44:45]
	global_load_dword v61, v23, s[44:45]
	global_load_dword v62, v24, s[44:45]
	global_load_dword v63, v25, s[44:45]
	s_add_u32 s44, s44, 0x30000
	s_addc_u32 s45, s45, 0
	ds_read_b128 v[68:71], v26 offset:32
	ds_read_b128 v[76:79], v27 offset:32
	s_waitcnt vmcnt(48)
	s_waitcnt lgkmcnt(2)
	v_mfma_f32_32x32x2_f32 v[32:47], v64, v80, v[32:47]
	v_mfma_f32_32x32x2_f32 v[32:47], v65, v81, v[32:47]
	v_mfma_f32_32x32x2_f32 v[32:47], v66, v82, v[32:47]
	v_mfma_f32_32x32x2_f32 v[32:47], v67, v83, v[32:47]
	v_fmac_f32_e32 v30, v72, v80
	v_fmac_f32_e32 v30, v73, v81
	v_fmac_f32_e32 v30, v74, v82
	v_fmac_f32_e32 v30, v75, v83
	ds_read_b128 v[64:67], v26 offset:64
	ds_read_b128 v[72:75], v27 offset:64
	s_waitcnt lgkmcnt(2)
	v_mfma_f32_32x32x2_f32 v[32:47], v68, v84, v[32:47]
	v_mfma_f32_32x32x2_f32 v[32:47], v69, v85, v[32:47]
	v_mfma_f32_32x32x2_f32 v[32:47], v70, v86, v[32:47]
	v_mfma_f32_32x32x2_f32 v[32:47], v71, v87, v[32:47]
	v_fmac_f32_e32 v30, v76, v84
	v_fmac_f32_e32 v30, v77, v85
	v_fmac_f32_e32 v30, v78, v86
	v_fmac_f32_e32 v30, v79, v87
	ds_read_b128 v[68:71], v26 offset:96
	ds_read_b128 v[76:79], v27 offset:96
	s_waitcnt lgkmcnt(2)
	v_mfma_f32_32x32x2_f32 v[32:47], v64, v88, v[32:47]
	v_mfma_f32_32x32x2_f32 v[32:47], v65, v89, v[32:47]
	v_mfma_f32_32x32x2_f32 v[32:47], v66, v90, v[32:47]
	v_mfma_f32_32x32x2_f32 v[32:47], v67, v91, v[32:47]
	v_fmac_f32_e32 v30, v72, v88
	v_fmac_f32_e32 v30, v73, v89
	v_fmac_f32_e32 v30, v74, v90
	v_fmac_f32_e32 v30, v75, v91
	ds_read_b128 v[64:67], v26 offset:128
	ds_read_b128 v[72:75], v27 offset:128
	s_waitcnt lgkmcnt(2)
	v_mfma_f32_32x32x2_f32 v[32:47], v68, v92, v[32:47]
	v_mfma_f32_32x32x2_f32 v[32:47], v69, v93, v[32:47]
	v_mfma_f32_32x32x2_f32 v[32:47], v70, v94, v[32:47]
	v_mfma_f32_32x32x2_f32 v[32:47], v71, v95, v[32:47]
	v_fmac_f32_e32 v30, v76, v92
	v_fmac_f32_e32 v30, v77, v93
	v_fmac_f32_e32 v30, v78, v94
	v_fmac_f32_e32 v30, v79, v95
	global_load_dword v80, v22, s[44:45]
	global_load_dword v81, v23, s[44:45]
	global_load_dword v82, v24, s[44:45]
	global_load_dword v83, v25, s[44:45]
	s_add_u32 s44, s44, 0x30000
	s_addc_u32 s45, s45, 0
	global_load_dword v84, v22, s[44:45]
	global_load_dword v85, v23, s[44:45]
	global_load_dword v86, v24, s[44:45]
	global_load_dword v87, v25, s[44:45]
	s_add_u32 s44, s44, 0x30000
	s_addc_u32 s45, s45, 0
	global_load_dword v88, v22, s[44:45]
	global_load_dword v89, v23, s[44:45]
	global_load_dword v90, v24, s[44:45]
	global_load_dword v91, v25, s[44:45]
	s_add_u32 s44, s44, 0x30000
	s_addc_u32 s45, s45, 0
	global_load_dword v92, v22, s[44:45]
	global_load_dword v93, v23, s[44:45]
	global_load_dword v94, v24, s[44:45]
	global_load_dword v95, v25, s[44:45]
	s_add_u32 s44, s44, 0x30000
	s_addc_u32 s45, s45, 0
	ds_read_b128 v[68:71], v26 offset:160
	ds_read_b128 v[76:79], v27 offset:160
	s_waitcnt vmcnt(48)
	s_waitcnt lgkmcnt(2)
	v_mfma_f32_32x32x2_f32 v[32:47], v64, v108, v[32:47]
	v_mfma_f32_32x32x2_f32 v[32:47], v65, v109, v[32:47]
	v_mfma_f32_32x32x2_f32 v[32:47], v66, v110, v[32:47]
	v_mfma_f32_32x32x2_f32 v[32:47], v67, v111, v[32:47]
	v_fmac_f32_e32 v30, v72, v108
	v_fmac_f32_e32 v30, v73, v109
	v_fmac_f32_e32 v30, v74, v110
	v_fmac_f32_e32 v30, v75, v111
	ds_read_b128 v[64:67], v26 offset:192
	ds_read_b128 v[72:75], v27 offset:192
	s_waitcnt lgkmcnt(2)
	v_mfma_f32_32x32x2_f32 v[32:47], v68, v112, v[32:47]
	v_mfma_f32_32x32x2_f32 v[32:47], v69, v113, v[32:47]
	v_mfma_f32_32x32x2_f32 v[32:47], v70, v114, v[32:47]
	v_mfma_f32_32x32x2_f32 v[32:47], v71, v115, v[32:47]
	v_fmac_f32_e32 v30, v76, v112
	v_fmac_f32_e32 v30, v77, v113
	v_fmac_f32_e32 v30, v78, v114
	v_fmac_f32_e32 v30, v79, v115
	ds_read_b128 v[68:71], v26 offset:224
	ds_read_b128 v[76:79], v27 offset:224
	s_waitcnt lgkmcnt(2)
	v_mfma_f32_32x32x2_f32 v[32:47], v64, v116, v[32:47]
	v_mfma_f32_32x32x2_f32 v[32:47], v65, v117, v[32:47]
	v_mfma_f32_32x32x2_f32 v[32:47], v66, v118, v[32:47]
	v_mfma_f32_32x32x2_f32 v[32:47], v67, v119, v[32:47]
	v_fmac_f32_e32 v30, v72, v116
	v_fmac_f32_e32 v30, v73, v117
	v_fmac_f32_e32 v30, v74, v118
	v_fmac_f32_e32 v30, v75, v119
	ds_read_b128 v[64:67], v26 offset:256
	ds_read_b128 v[72:75], v27 offset:256
	s_waitcnt lgkmcnt(2)
	v_mfma_f32_32x32x2_f32 v[32:47], v68, v120, v[32:47]
	v_mfma_f32_32x32x2_f32 v[32:47], v69, v121, v[32:47]
	v_mfma_f32_32x32x2_f32 v[32:47], v70, v122, v[32:47]
	v_mfma_f32_32x32x2_f32 v[32:47], v71, v123, v[32:47]
	v_fmac_f32_e32 v30, v76, v120
	v_fmac_f32_e32 v30, v77, v121
	v_fmac_f32_e32 v30, v78, v122
	v_fmac_f32_e32 v30, v79, v123
	global_load_dword v108, v22, s[44:45]
	global_load_dword v109, v23, s[44:45]
	global_load_dword v110, v24, s[44:45]
	global_load_dword v111, v25, s[44:45]
	s_add_u32 s44, s44, 0x30000
	s_addc_u32 s45, s45, 0
	global_load_dword v112, v22, s[44:45]
	global_load_dword v113, v23, s[44:45]
	global_load_dword v114, v24, s[44:45]
	global_load_dword v115, v25, s[44:45]
	s_add_u32 s44, s44, 0x30000
	s_addc_u32 s45, s45, 0
	global_load_dword v116, v22, s[44:45]
	global_load_dword v117, v23, s[44:45]
	global_load_dword v118, v24, s[44:45]
	global_load_dword v119, v25, s[44:45]
	s_add_u32 s44, s44, 0x30000
	s_addc_u32 s45, s45, 0
	global_load_dword v120, v22, s[44:45]
	global_load_dword v121, v23, s[44:45]
	global_load_dword v122, v24, s[44:45]
	global_load_dword v123, v25, s[44:45]
	s_add_u32 s44, s44, 0x30000
	s_addc_u32 s45, s45, 0
	ds_read_b128 v[68:71], v26 offset:288
	ds_read_b128 v[76:79], v27 offset:288
	s_waitcnt vmcnt(48)
	s_waitcnt lgkmcnt(2)
	v_mfma_f32_32x32x2_f32 v[32:47], v64, v124, v[32:47]
	v_mfma_f32_32x32x2_f32 v[32:47], v65, v125, v[32:47]
	v_mfma_f32_32x32x2_f32 v[32:47], v66, v126, v[32:47]
	v_mfma_f32_32x32x2_f32 v[32:47], v67, v127, v[32:47]
	v_fmac_f32_e32 v30, v72, v124
	v_fmac_f32_e32 v30, v73, v125
	v_fmac_f32_e32 v30, v74, v126
	v_fmac_f32_e32 v30, v75, v127
	ds_read_b128 v[64:67], v26 offset:320
	ds_read_b128 v[72:75], v27 offset:320
	s_waitcnt lgkmcnt(2)
	v_mfma_f32_32x32x2_f32 v[32:47], v68, v128, v[32:47]
	v_mfma_f32_32x32x2_f32 v[32:47], v69, v129, v[32:47]
	v_mfma_f32_32x32x2_f32 v[32:47], v70, v130, v[32:47]
	v_mfma_f32_32x32x2_f32 v[32:47], v71, v131, v[32:47]
	v_fmac_f32_e32 v30, v76, v128
	v_fmac_f32_e32 v30, v77, v129
	v_fmac_f32_e32 v30, v78, v130
	v_fmac_f32_e32 v30, v79, v131
	ds_read_b128 v[68:71], v26 offset:352
	ds_read_b128 v[76:79], v27 offset:352
	s_waitcnt lgkmcnt(2)
	v_mfma_f32_32x32x2_f32 v[32:47], v64, v132, v[32:47]
	v_mfma_f32_32x32x2_f32 v[32:47], v65, v133, v[32:47]
	v_mfma_f32_32x32x2_f32 v[32:47], v66, v134, v[32:47]
	v_mfma_f32_32x32x2_f32 v[32:47], v67, v135, v[32:47]
	v_fmac_f32_e32 v30, v72, v132
	v_fmac_f32_e32 v30, v73, v133
	v_fmac_f32_e32 v30, v74, v134
	v_fmac_f32_e32 v30, v75, v135
	ds_read_b128 v[64:67], v26 offset:384
	ds_read_b128 v[72:75], v27 offset:384
	s_waitcnt lgkmcnt(2)
	v_mfma_f32_32x32x2_f32 v[32:47], v68, v136, v[32:47]
	v_mfma_f32_32x32x2_f32 v[32:47], v69, v137, v[32:47]
	v_mfma_f32_32x32x2_f32 v[32:47], v70, v138, v[32:47]
	v_mfma_f32_32x32x2_f32 v[32:47], v71, v139, v[32:47]
	v_fmac_f32_e32 v30, v76, v136
	v_fmac_f32_e32 v30, v77, v137
	v_fmac_f32_e32 v30, v78, v138
	v_fmac_f32_e32 v30, v79, v139
	global_load_dword v124, v22, s[44:45]
	global_load_dword v125, v23, s[44:45]
	global_load_dword v126, v24, s[44:45]
	global_load_dword v127, v25, s[44:45]
	s_add_u32 s44, s44, 0x30000
	s_addc_u32 s45, s45, 0
	global_load_dword v128, v22, s[44:45]
	global_load_dword v129, v23, s[44:45]
	global_load_dword v130, v24, s[44:45]
	global_load_dword v131, v25, s[44:45]
	s_add_u32 s44, s44, 0x30000
	s_addc_u32 s45, s45, 0
	global_load_dword v132, v22, s[44:45]
	global_load_dword v133, v23, s[44:45]
	global_load_dword v134, v24, s[44:45]
	global_load_dword v135, v25, s[44:45]
	s_add_u32 s44, s44, 0x30000
	s_addc_u32 s45, s45, 0
	global_load_dword v136, v22, s[44:45]
	global_load_dword v137, v23, s[44:45]
	global_load_dword v138, v24, s[44:45]
	global_load_dword v139, v25, s[44:45]
	s_add_u32 s44, s44, 0x30000
	s_addc_u32 s45, s45, 0
	ds_read_b128 v[68:71], v26 offset:416
	ds_read_b128 v[76:79], v27 offset:416
	s_waitcnt vmcnt(48)
	s_waitcnt lgkmcnt(2)
	v_mfma_f32_32x32x2_f32 v[32:47], v64, v48, v[32:47]
	v_mfma_f32_32x32x2_f32 v[32:47], v65, v49, v[32:47]
	v_mfma_f32_32x32x2_f32 v[32:47], v66, v50, v[32:47]
	v_mfma_f32_32x32x2_f32 v[32:47], v67, v51, v[32:47]
	v_fmac_f32_e32 v30, v72, v48
	v_fmac_f32_e32 v30, v73, v49
	v_fmac_f32_e32 v30, v74, v50
	v_fmac_f32_e32 v30, v75, v51
	ds_read_b128 v[64:67], v26 offset:448
	ds_read_b128 v[72:75], v27 offset:448
	s_waitcnt lgkmcnt(2)
	v_mfma_f32_32x32x2_f32 v[32:47], v68, v52, v[32:47]
	v_mfma_f32_32x32x2_f32 v[32:47], v69, v53, v[32:47]
	v_mfma_f32_32x32x2_f32 v[32:47], v70, v54, v[32:47]
	v_mfma_f32_32x32x2_f32 v[32:47], v71, v55, v[32:47]
	v_fmac_f32_e32 v30, v76, v52
	v_fmac_f32_e32 v30, v77, v53
	v_fmac_f32_e32 v30, v78, v54
	v_fmac_f32_e32 v30, v79, v55
	ds_read_b128 v[68:71], v26 offset:480
	ds_read_b128 v[76:79], v27 offset:480
	s_waitcnt lgkmcnt(2)
	v_mfma_f32_32x32x2_f32 v[32:47], v64, v56, v[32:47]
	v_mfma_f32_32x32x2_f32 v[32:47], v65, v57, v[32:47]
	v_mfma_f32_32x32x2_f32 v[32:47], v66, v58, v[32:47]
	v_mfma_f32_32x32x2_f32 v[32:47], v67, v59, v[32:47]
	v_fmac_f32_e32 v30, v72, v56
	v_fmac_f32_e32 v30, v73, v57
	v_fmac_f32_e32 v30, v74, v58
	v_fmac_f32_e32 v30, v75, v59
	ds_read_b128 v[64:67], v26 offset:512
	ds_read_b128 v[72:75], v27 offset:512
	s_waitcnt lgkmcnt(2)
	v_mfma_f32_32x32x2_f32 v[32:47], v68, v60, v[32:47]
	v_mfma_f32_32x32x2_f32 v[32:47], v69, v61, v[32:47]
	v_mfma_f32_32x32x2_f32 v[32:47], v70, v62, v[32:47]
	v_mfma_f32_32x32x2_f32 v[32:47], v71, v63, v[32:47]
	v_fmac_f32_e32 v30, v76, v60
	v_fmac_f32_e32 v30, v77, v61
	v_fmac_f32_e32 v30, v78, v62
	v_fmac_f32_e32 v30, v79, v63
	global_load_dword v48, v22, s[44:45]
	global_load_dword v49, v23, s[44:45]
	global_load_dword v50, v24, s[44:45]
	global_load_dword v51, v25, s[44:45]
	s_add_u32 s44, s44, 0x30000
	s_addc_u32 s45, s45, 0
	global_load_dword v52, v22, s[44:45]
	global_load_dword v53, v23, s[44:45]
	global_load_dword v54, v24, s[44:45]
	global_load_dword v55, v25, s[44:45]
	s_add_u32 s44, s44, 0x30000
	s_addc_u32 s45, s45, 0
	global_load_dword v56, v22, s[44:45]
	global_load_dword v57, v23, s[44:45]
	global_load_dword v58, v24, s[44:45]
	global_load_dword v59, v25, s[44:45]
	s_add_u32 s44, s44, 0x30000
	s_addc_u32 s45, s45, 0
	global_load_dword v60, v22, s[44:45]
	global_load_dword v61, v23, s[44:45]
	global_load_dword v62, v24, s[44:45]
	global_load_dword v63, v25, s[44:45]
	s_add_u32 s44, s44, 0x30000
	s_addc_u32 s45, s45, 0
	ds_read_b128 v[68:71], v26 offset:544
	ds_read_b128 v[76:79], v27 offset:544
	s_waitcnt vmcnt(48)
	s_waitcnt lgkmcnt(2)
	v_mfma_f32_32x32x2_f32 v[32:47], v64, v80, v[32:47]
	v_mfma_f32_32x32x2_f32 v[32:47], v65, v81, v[32:47]
	v_mfma_f32_32x32x2_f32 v[32:47], v66, v82, v[32:47]
	v_mfma_f32_32x32x2_f32 v[32:47], v67, v83, v[32:47]
	v_fmac_f32_e32 v30, v72, v80
	v_fmac_f32_e32 v30, v73, v81
	v_fmac_f32_e32 v30, v74, v82
	v_fmac_f32_e32 v30, v75, v83
	ds_read_b128 v[64:67], v26 offset:576
	ds_read_b128 v[72:75], v27 offset:576
	s_waitcnt lgkmcnt(2)
	v_mfma_f32_32x32x2_f32 v[32:47], v68, v84, v[32:47]
	v_mfma_f32_32x32x2_f32 v[32:47], v69, v85, v[32:47]
	v_mfma_f32_32x32x2_f32 v[32:47], v70, v86, v[32:47]
	v_mfma_f32_32x32x2_f32 v[32:47], v71, v87, v[32:47]
	v_fmac_f32_e32 v30, v76, v84
	v_fmac_f32_e32 v30, v77, v85
	v_fmac_f32_e32 v30, v78, v86
	v_fmac_f32_e32 v30, v79, v87
	ds_read_b128 v[68:71], v26 offset:608
	ds_read_b128 v[76:79], v27 offset:608
	s_waitcnt lgkmcnt(2)
	v_mfma_f32_32x32x2_f32 v[32:47], v64, v88, v[32:47]
	v_mfma_f32_32x32x2_f32 v[32:47], v65, v89, v[32:47]
	v_mfma_f32_32x32x2_f32 v[32:47], v66, v90, v[32:47]
	v_mfma_f32_32x32x2_f32 v[32:47], v67, v91, v[32:47]
	v_fmac_f32_e32 v30, v72, v88
	v_fmac_f32_e32 v30, v73, v89
	v_fmac_f32_e32 v30, v74, v90
	v_fmac_f32_e32 v30, v75, v91
	ds_read_b128 v[64:67], v26 offset:640
	ds_read_b128 v[72:75], v27 offset:640
	s_waitcnt lgkmcnt(2)
	v_mfma_f32_32x32x2_f32 v[32:47], v68, v92, v[32:47]
	v_mfma_f32_32x32x2_f32 v[32:47], v69, v93, v[32:47]
	v_mfma_f32_32x32x2_f32 v[32:47], v70, v94, v[32:47]
	v_mfma_f32_32x32x2_f32 v[32:47], v71, v95, v[32:47]
	v_fmac_f32_e32 v30, v76, v92
	v_fmac_f32_e32 v30, v77, v93
	v_fmac_f32_e32 v30, v78, v94
	v_fmac_f32_e32 v30, v79, v95
	global_load_dword v80, v22, s[44:45]
	global_load_dword v81, v23, s[44:45]
	global_load_dword v82, v24, s[44:45]
	global_load_dword v83, v25, s[44:45]
	s_add_u32 s44, s44, 0x30000
	s_addc_u32 s45, s45, 0
	global_load_dword v84, v22, s[44:45]
	global_load_dword v85, v23, s[44:45]
	global_load_dword v86, v24, s[44:45]
	global_load_dword v87, v25, s[44:45]
	s_add_u32 s44, s44, 0x30000
	s_addc_u32 s45, s45, 0
	global_load_dword v88, v22, s[44:45]
	global_load_dword v89, v23, s[44:45]
	global_load_dword v90, v24, s[44:45]
	global_load_dword v91, v25, s[44:45]
	s_add_u32 s44, s44, 0x30000
	s_addc_u32 s45, s45, 0
	global_load_dword v92, v22, s[44:45]
	global_load_dword v93, v23, s[44:45]
	global_load_dword v94, v24, s[44:45]
	global_load_dword v95, v25, s[44:45]
	s_add_u32 s44, s44, 0x30000
	s_addc_u32 s45, s45, 0
	ds_read_b128 v[68:71], v26 offset:672
	ds_read_b128 v[76:79], v27 offset:672
	s_waitcnt vmcnt(48)
	s_waitcnt lgkmcnt(2)
	v_mfma_f32_32x32x2_f32 v[32:47], v64, v108, v[32:47]
	v_mfma_f32_32x32x2_f32 v[32:47], v65, v109, v[32:47]
	v_mfma_f32_32x32x2_f32 v[32:47], v66, v110, v[32:47]
	v_mfma_f32_32x32x2_f32 v[32:47], v67, v111, v[32:47]
	v_fmac_f32_e32 v30, v72, v108
	v_fmac_f32_e32 v30, v73, v109
	v_fmac_f32_e32 v30, v74, v110
	v_fmac_f32_e32 v30, v75, v111
	ds_read_b128 v[64:67], v26 offset:704
	ds_read_b128 v[72:75], v27 offset:704
	s_waitcnt lgkmcnt(2)
	v_mfma_f32_32x32x2_f32 v[32:47], v68, v112, v[32:47]
	v_mfma_f32_32x32x2_f32 v[32:47], v69, v113, v[32:47]
	v_mfma_f32_32x32x2_f32 v[32:47], v70, v114, v[32:47]
	v_mfma_f32_32x32x2_f32 v[32:47], v71, v115, v[32:47]
	v_fmac_f32_e32 v30, v76, v112
	v_fmac_f32_e32 v30, v77, v113
	v_fmac_f32_e32 v30, v78, v114
	v_fmac_f32_e32 v30, v79, v115
	ds_read_b128 v[68:71], v26 offset:736
	ds_read_b128 v[76:79], v27 offset:736
	s_waitcnt lgkmcnt(2)
	v_mfma_f32_32x32x2_f32 v[32:47], v64, v116, v[32:47]
	v_mfma_f32_32x32x2_f32 v[32:47], v65, v117, v[32:47]
	v_mfma_f32_32x32x2_f32 v[32:47], v66, v118, v[32:47]
	v_mfma_f32_32x32x2_f32 v[32:47], v67, v119, v[32:47]
	v_fmac_f32_e32 v30, v72, v116
	v_fmac_f32_e32 v30, v73, v117
	v_fmac_f32_e32 v30, v74, v118
	v_fmac_f32_e32 v30, v75, v119
	ds_read_b128 v[64:67], v26 offset:768
	ds_read_b128 v[72:75], v27 offset:768
	s_waitcnt lgkmcnt(2)
	v_mfma_f32_32x32x2_f32 v[32:47], v68, v120, v[32:47]
	v_mfma_f32_32x32x2_f32 v[32:47], v69, v121, v[32:47]
	v_mfma_f32_32x32x2_f32 v[32:47], v70, v122, v[32:47]
	v_mfma_f32_32x32x2_f32 v[32:47], v71, v123, v[32:47]
	v_fmac_f32_e32 v30, v76, v120
	v_fmac_f32_e32 v30, v77, v121
	v_fmac_f32_e32 v30, v78, v122
	v_fmac_f32_e32 v30, v79, v123
	global_load_dword v108, v22, s[44:45]
	global_load_dword v109, v23, s[44:45]
	global_load_dword v110, v24, s[44:45]
	global_load_dword v111, v25, s[44:45]
	s_add_u32 s44, s44, 0x30000
	s_addc_u32 s45, s45, 0
	global_load_dword v112, v22, s[44:45]
	global_load_dword v113, v23, s[44:45]
	global_load_dword v114, v24, s[44:45]
	global_load_dword v115, v25, s[44:45]
	s_add_u32 s44, s44, 0x30000
	s_addc_u32 s45, s45, 0
	global_load_dword v116, v22, s[44:45]
	global_load_dword v117, v23, s[44:45]
	global_load_dword v118, v24, s[44:45]
	global_load_dword v119, v25, s[44:45]
	s_add_u32 s44, s44, 0x30000
	s_addc_u32 s45, s45, 0
	global_load_dword v120, v22, s[44:45]
	global_load_dword v121, v23, s[44:45]
	global_load_dword v122, v24, s[44:45]
	global_load_dword v123, v25, s[44:45]
	s_add_u32 s44, s44, 0x30000
	s_addc_u32 s45, s45, 0
	ds_read_b128 v[68:71], v26 offset:800
	ds_read_b128 v[76:79], v27 offset:800
	s_waitcnt vmcnt(48)
	s_waitcnt lgkmcnt(2)
	v_mfma_f32_32x32x2_f32 v[32:47], v64, v124, v[32:47]
	v_mfma_f32_32x32x2_f32 v[32:47], v65, v125, v[32:47]
	v_mfma_f32_32x32x2_f32 v[32:47], v66, v126, v[32:47]
	v_mfma_f32_32x32x2_f32 v[32:47], v67, v127, v[32:47]
	v_fmac_f32_e32 v30, v72, v124
	v_fmac_f32_e32 v30, v73, v125
	v_fmac_f32_e32 v30, v74, v126
	v_fmac_f32_e32 v30, v75, v127
	ds_read_b128 v[64:67], v26 offset:832
	ds_read_b128 v[72:75], v27 offset:832
	s_waitcnt lgkmcnt(2)
	v_mfma_f32_32x32x2_f32 v[32:47], v68, v128, v[32:47]
	v_mfma_f32_32x32x2_f32 v[32:47], v69, v129, v[32:47]
	v_mfma_f32_32x32x2_f32 v[32:47], v70, v130, v[32:47]
	v_mfma_f32_32x32x2_f32 v[32:47], v71, v131, v[32:47]
	v_fmac_f32_e32 v30, v76, v128
	v_fmac_f32_e32 v30, v77, v129
	v_fmac_f32_e32 v30, v78, v130
	v_fmac_f32_e32 v30, v79, v131
	ds_read_b128 v[68:71], v26 offset:864
	ds_read_b128 v[76:79], v27 offset:864
	s_waitcnt lgkmcnt(2)
	v_mfma_f32_32x32x2_f32 v[32:47], v64, v132, v[32:47]
	v_mfma_f32_32x32x2_f32 v[32:47], v65, v133, v[32:47]
	v_mfma_f32_32x32x2_f32 v[32:47], v66, v134, v[32:47]
	v_mfma_f32_32x32x2_f32 v[32:47], v67, v135, v[32:47]
	v_fmac_f32_e32 v30, v72, v132
	v_fmac_f32_e32 v30, v73, v133
	v_fmac_f32_e32 v30, v74, v134
	v_fmac_f32_e32 v30, v75, v135
	ds_read_b128 v[64:67], v26 offset:896
	ds_read_b128 v[72:75], v27 offset:896
	s_waitcnt lgkmcnt(2)
	v_mfma_f32_32x32x2_f32 v[32:47], v68, v136, v[32:47]
	v_mfma_f32_32x32x2_f32 v[32:47], v69, v137, v[32:47]
	v_mfma_f32_32x32x2_f32 v[32:47], v70, v138, v[32:47]
	v_mfma_f32_32x32x2_f32 v[32:47], v71, v139, v[32:47]
	v_fmac_f32_e32 v30, v76, v136
	v_fmac_f32_e32 v30, v77, v137
	v_fmac_f32_e32 v30, v78, v138
	v_fmac_f32_e32 v30, v79, v139
	global_load_dword v124, v22, s[44:45]
	global_load_dword v125, v23, s[44:45]
	global_load_dword v126, v24, s[44:45]
	global_load_dword v127, v25, s[44:45]
	s_add_u32 s44, s44, 0x30000
	s_addc_u32 s45, s45, 0
	global_load_dword v128, v22, s[44:45]
	global_load_dword v129, v23, s[44:45]
	global_load_dword v130, v24, s[44:45]
	global_load_dword v131, v25, s[44:45]
	s_add_u32 s44, s44, 0x30000
	s_addc_u32 s45, s45, 0
	global_load_dword v132, v22, s[44:45]
	global_load_dword v133, v23, s[44:45]
	global_load_dword v134, v24, s[44:45]
	global_load_dword v135, v25, s[44:45]
	s_add_u32 s44, s44, 0x30000
	s_addc_u32 s45, s45, 0
	global_load_dword v136, v22, s[44:45]
	global_load_dword v137, v23, s[44:45]
	global_load_dword v138, v24, s[44:45]
	global_load_dword v139, v25, s[44:45]
	s_add_u32 s44, s44, 0x30000
	s_addc_u32 s45, s45, 0
	ds_read_b128 v[68:71], v26 offset:928
	ds_read_b128 v[76:79], v27 offset:928
	s_waitcnt vmcnt(48)
	s_waitcnt lgkmcnt(2)
	v_mfma_f32_32x32x2_f32 v[32:47], v64, v48, v[32:47]
	v_mfma_f32_32x32x2_f32 v[32:47], v65, v49, v[32:47]
	v_mfma_f32_32x32x2_f32 v[32:47], v66, v50, v[32:47]
	v_mfma_f32_32x32x2_f32 v[32:47], v67, v51, v[32:47]
	v_fmac_f32_e32 v30, v72, v48
	v_fmac_f32_e32 v30, v73, v49
	v_fmac_f32_e32 v30, v74, v50
	v_fmac_f32_e32 v30, v75, v51
	ds_read_b128 v[64:67], v26 offset:960
	ds_read_b128 v[72:75], v27 offset:960
	s_waitcnt lgkmcnt(2)
	v_mfma_f32_32x32x2_f32 v[32:47], v68, v52, v[32:47]
	v_mfma_f32_32x32x2_f32 v[32:47], v69, v53, v[32:47]
	v_mfma_f32_32x32x2_f32 v[32:47], v70, v54, v[32:47]
	v_mfma_f32_32x32x2_f32 v[32:47], v71, v55, v[32:47]
	v_fmac_f32_e32 v30, v76, v52
	v_fmac_f32_e32 v30, v77, v53
	v_fmac_f32_e32 v30, v78, v54
	v_fmac_f32_e32 v30, v79, v55
	ds_read_b128 v[68:71], v26 offset:992
	ds_read_b128 v[76:79], v27 offset:992
	s_waitcnt lgkmcnt(2)
	v_mfma_f32_32x32x2_f32 v[32:47], v64, v56, v[32:47]
	v_mfma_f32_32x32x2_f32 v[32:47], v65, v57, v[32:47]
	v_mfma_f32_32x32x2_f32 v[32:47], v66, v58, v[32:47]
	v_mfma_f32_32x32x2_f32 v[32:47], v67, v59, v[32:47]
	v_fmac_f32_e32 v30, v72, v56
	v_fmac_f32_e32 v30, v73, v57
	v_fmac_f32_e32 v30, v74, v58
	v_fmac_f32_e32 v30, v75, v59
	ds_read_b128 v[64:67], v26 offset:1024
	ds_read_b128 v[72:75], v27 offset:1024
	s_waitcnt lgkmcnt(2)
	v_mfma_f32_32x32x2_f32 v[32:47], v68, v60, v[32:47]
	v_mfma_f32_32x32x2_f32 v[32:47], v69, v61, v[32:47]
	v_mfma_f32_32x32x2_f32 v[32:47], v70, v62, v[32:47]
	v_mfma_f32_32x32x2_f32 v[32:47], v71, v63, v[32:47]
	v_fmac_f32_e32 v30, v76, v60
	v_fmac_f32_e32 v30, v77, v61
	v_fmac_f32_e32 v30, v78, v62
	v_fmac_f32_e32 v30, v79, v63
	global_load_dword v48, v22, s[44:45]
	global_load_dword v49, v23, s[44:45]
	global_load_dword v50, v24, s[44:45]
	global_load_dword v51, v25, s[44:45]
	s_add_u32 s44, s44, 0x30000
	s_addc_u32 s45, s45, 0
	global_load_dword v52, v22, s[44:45]
	global_load_dword v53, v23, s[44:45]
	global_load_dword v54, v24, s[44:45]
	global_load_dword v55, v25, s[44:45]
	s_add_u32 s44, s44, 0x30000
	s_addc_u32 s45, s45, 0
	global_load_dword v56, v22, s[44:45]
	global_load_dword v57, v23, s[44:45]
	global_load_dword v58, v24, s[44:45]
	global_load_dword v59, v25, s[44:45]
	s_add_u32 s44, s44, 0x30000
	s_addc_u32 s45, s45, 0
	global_load_dword v60, v22, s[44:45]
	global_load_dword v61, v23, s[44:45]
	global_load_dword v62, v24, s[44:45]
	global_load_dword v63, v25, s[44:45]
	s_add_u32 s44, s44, 0x30000
	s_addc_u32 s45, s45, 0
	ds_read_b128 v[68:71], v26 offset:1056
	ds_read_b128 v[76:79], v27 offset:1056
	s_waitcnt vmcnt(48)
	s_waitcnt lgkmcnt(2)
	v_mfma_f32_32x32x2_f32 v[32:47], v64, v80, v[32:47]
	v_mfma_f32_32x32x2_f32 v[32:47], v65, v81, v[32:47]
	v_mfma_f32_32x32x2_f32 v[32:47], v66, v82, v[32:47]
	v_mfma_f32_32x32x2_f32 v[32:47], v67, v83, v[32:47]
	v_fmac_f32_e32 v30, v72, v80
	v_fmac_f32_e32 v30, v73, v81
	v_fmac_f32_e32 v30, v74, v82
	v_fmac_f32_e32 v30, v75, v83
	ds_read_b128 v[64:67], v26 offset:1088
	ds_read_b128 v[72:75], v27 offset:1088
	s_waitcnt lgkmcnt(2)
	v_mfma_f32_32x32x2_f32 v[32:47], v68, v84, v[32:47]
	v_mfma_f32_32x32x2_f32 v[32:47], v69, v85, v[32:47]
	v_mfma_f32_32x32x2_f32 v[32:47], v70, v86, v[32:47]
	v_mfma_f32_32x32x2_f32 v[32:47], v71, v87, v[32:47]
	v_fmac_f32_e32 v30, v76, v84
	v_fmac_f32_e32 v30, v77, v85
	v_fmac_f32_e32 v30, v78, v86
	v_fmac_f32_e32 v30, v79, v87
	ds_read_b128 v[68:71], v26 offset:1120
	ds_read_b128 v[76:79], v27 offset:1120
	s_waitcnt lgkmcnt(2)
	v_mfma_f32_32x32x2_f32 v[32:47], v64, v88, v[32:47]
	v_mfma_f32_32x32x2_f32 v[32:47], v65, v89, v[32:47]
	v_mfma_f32_32x32x2_f32 v[32:47], v66, v90, v[32:47]
	v_mfma_f32_32x32x2_f32 v[32:47], v67, v91, v[32:47]
	v_fmac_f32_e32 v30, v72, v88
	v_fmac_f32_e32 v30, v73, v89
	v_fmac_f32_e32 v30, v74, v90
	v_fmac_f32_e32 v30, v75, v91
	ds_read_b128 v[64:67], v26 offset:1152
	ds_read_b128 v[72:75], v27 offset:1152
	s_waitcnt lgkmcnt(2)
	v_mfma_f32_32x32x2_f32 v[32:47], v68, v92, v[32:47]
	v_mfma_f32_32x32x2_f32 v[32:47], v69, v93, v[32:47]
	v_mfma_f32_32x32x2_f32 v[32:47], v70, v94, v[32:47]
	v_mfma_f32_32x32x2_f32 v[32:47], v71, v95, v[32:47]
	v_fmac_f32_e32 v30, v76, v92
	v_fmac_f32_e32 v30, v77, v93
	v_fmac_f32_e32 v30, v78, v94
	v_fmac_f32_e32 v30, v79, v95
	global_load_dword v80, v22, s[44:45]
	global_load_dword v81, v23, s[44:45]
	global_load_dword v82, v24, s[44:45]
	global_load_dword v83, v25, s[44:45]
	s_add_u32 s44, s44, 0x30000
	s_addc_u32 s45, s45, 0
	global_load_dword v84, v22, s[44:45]
	global_load_dword v85, v23, s[44:45]
	global_load_dword v86, v24, s[44:45]
	global_load_dword v87, v25, s[44:45]
	s_add_u32 s44, s44, 0x30000
	s_addc_u32 s45, s45, 0
	global_load_dword v88, v22, s[44:45]
	global_load_dword v89, v23, s[44:45]
	global_load_dword v90, v24, s[44:45]
	global_load_dword v91, v25, s[44:45]
	s_add_u32 s44, s44, 0x30000
	s_addc_u32 s45, s45, 0
	global_load_dword v92, v22, s[44:45]
	global_load_dword v93, v23, s[44:45]
	global_load_dword v94, v24, s[44:45]
	global_load_dword v95, v25, s[44:45]
	s_add_u32 s44, s44, 0x30000
	s_addc_u32 s45, s45, 0
	ds_read_b128 v[68:71], v26 offset:1184
	ds_read_b128 v[76:79], v27 offset:1184
	s_waitcnt vmcnt(48)
	s_waitcnt lgkmcnt(2)
	v_mfma_f32_32x32x2_f32 v[32:47], v64, v108, v[32:47]
	v_mfma_f32_32x32x2_f32 v[32:47], v65, v109, v[32:47]
	v_mfma_f32_32x32x2_f32 v[32:47], v66, v110, v[32:47]
	v_mfma_f32_32x32x2_f32 v[32:47], v67, v111, v[32:47]
	v_fmac_f32_e32 v30, v72, v108
	v_fmac_f32_e32 v30, v73, v109
	v_fmac_f32_e32 v30, v74, v110
	v_fmac_f32_e32 v30, v75, v111
	ds_read_b128 v[64:67], v26 offset:1216
	ds_read_b128 v[72:75], v27 offset:1216
	s_waitcnt lgkmcnt(2)
	v_mfma_f32_32x32x2_f32 v[32:47], v68, v112, v[32:47]
	v_mfma_f32_32x32x2_f32 v[32:47], v69, v113, v[32:47]
	v_mfma_f32_32x32x2_f32 v[32:47], v70, v114, v[32:47]
	v_mfma_f32_32x32x2_f32 v[32:47], v71, v115, v[32:47]
	v_fmac_f32_e32 v30, v76, v112
	v_fmac_f32_e32 v30, v77, v113
	v_fmac_f32_e32 v30, v78, v114
	v_fmac_f32_e32 v30, v79, v115
	ds_read_b128 v[68:71], v26 offset:1248
	ds_read_b128 v[76:79], v27 offset:1248
	s_waitcnt lgkmcnt(2)
	v_mfma_f32_32x32x2_f32 v[32:47], v64, v116, v[32:47]
	v_mfma_f32_32x32x2_f32 v[32:47], v65, v117, v[32:47]
	v_mfma_f32_32x32x2_f32 v[32:47], v66, v118, v[32:47]
	v_mfma_f32_32x32x2_f32 v[32:47], v67, v119, v[32:47]
	v_fmac_f32_e32 v30, v72, v116
	v_fmac_f32_e32 v30, v73, v117
	v_fmac_f32_e32 v30, v74, v118
	v_fmac_f32_e32 v30, v75, v119
	ds_read_b128 v[64:67], v26 offset:1280
	ds_read_b128 v[72:75], v27 offset:1280
	s_waitcnt lgkmcnt(2)
	v_mfma_f32_32x32x2_f32 v[32:47], v68, v120, v[32:47]
	v_mfma_f32_32x32x2_f32 v[32:47], v69, v121, v[32:47]
	v_mfma_f32_32x32x2_f32 v[32:47], v70, v122, v[32:47]
	v_mfma_f32_32x32x2_f32 v[32:47], v71, v123, v[32:47]
	v_fmac_f32_e32 v30, v76, v120
	v_fmac_f32_e32 v30, v77, v121
	v_fmac_f32_e32 v30, v78, v122
	v_fmac_f32_e32 v30, v79, v123
	global_load_dword v108, v22, s[44:45]
	global_load_dword v109, v23, s[44:45]
	global_load_dword v110, v24, s[44:45]
	global_load_dword v111, v25, s[44:45]
	s_add_u32 s44, s44, 0x30000
	s_addc_u32 s45, s45, 0
	global_load_dword v112, v22, s[44:45]
	global_load_dword v113, v23, s[44:45]
	global_load_dword v114, v24, s[44:45]
	global_load_dword v115, v25, s[44:45]
	s_add_u32 s44, s44, 0x30000
	s_addc_u32 s45, s45, 0
	global_load_dword v116, v22, s[44:45]
	global_load_dword v117, v23, s[44:45]
	global_load_dword v118, v24, s[44:45]
	global_load_dword v119, v25, s[44:45]
	s_add_u32 s44, s44, 0x30000
	s_addc_u32 s45, s45, 0
	global_load_dword v120, v22, s[44:45]
	global_load_dword v121, v23, s[44:45]
	global_load_dword v122, v24, s[44:45]
	global_load_dword v123, v25, s[44:45]
	s_add_u32 s44, s44, 0x30000
	s_addc_u32 s45, s45, 0
	ds_read_b128 v[68:71], v26 offset:1312
	ds_read_b128 v[76:79], v27 offset:1312
	s_waitcnt vmcnt(48)
	s_waitcnt lgkmcnt(2)
	v_mfma_f32_32x32x2_f32 v[32:47], v64, v124, v[32:47]
	v_mfma_f32_32x32x2_f32 v[32:47], v65, v125, v[32:47]
	v_mfma_f32_32x32x2_f32 v[32:47], v66, v126, v[32:47]
	v_mfma_f32_32x32x2_f32 v[32:47], v67, v127, v[32:47]
	v_fmac_f32_e32 v30, v72, v124
	v_fmac_f32_e32 v30, v73, v125
	v_fmac_f32_e32 v30, v74, v126
	v_fmac_f32_e32 v30, v75, v127
	ds_read_b128 v[64:67], v26 offset:1344
	ds_read_b128 v[72:75], v27 offset:1344
	s_waitcnt lgkmcnt(2)
	v_mfma_f32_32x32x2_f32 v[32:47], v68, v128, v[32:47]
	v_mfma_f32_32x32x2_f32 v[32:47], v69, v129, v[32:47]
	v_mfma_f32_32x32x2_f32 v[32:47], v70, v130, v[32:47]
	v_mfma_f32_32x32x2_f32 v[32:47], v71, v131, v[32:47]
	v_fmac_f32_e32 v30, v76, v128
	v_fmac_f32_e32 v30, v77, v129
	v_fmac_f32_e32 v30, v78, v130
	v_fmac_f32_e32 v30, v79, v131
	ds_read_b128 v[68:71], v26 offset:1376
	ds_read_b128 v[76:79], v27 offset:1376
	s_waitcnt lgkmcnt(2)
	v_mfma_f32_32x32x2_f32 v[32:47], v64, v132, v[32:47]
	v_mfma_f32_32x32x2_f32 v[32:47], v65, v133, v[32:47]
	v_mfma_f32_32x32x2_f32 v[32:47], v66, v134, v[32:47]
	v_mfma_f32_32x32x2_f32 v[32:47], v67, v135, v[32:47]
	v_fmac_f32_e32 v30, v72, v132
	v_fmac_f32_e32 v30, v73, v133
	v_fmac_f32_e32 v30, v74, v134
	v_fmac_f32_e32 v30, v75, v135
	ds_read_b128 v[64:67], v26 offset:1408
	ds_read_b128 v[72:75], v27 offset:1408
	s_waitcnt lgkmcnt(2)
	v_mfma_f32_32x32x2_f32 v[32:47], v68, v136, v[32:47]
	v_mfma_f32_32x32x2_f32 v[32:47], v69, v137, v[32:47]
	v_mfma_f32_32x32x2_f32 v[32:47], v70, v138, v[32:47]
	v_mfma_f32_32x32x2_f32 v[32:47], v71, v139, v[32:47]
	v_fmac_f32_e32 v30, v76, v136
	v_fmac_f32_e32 v30, v77, v137
	v_fmac_f32_e32 v30, v78, v138
	v_fmac_f32_e32 v30, v79, v139
	global_load_dword v124, v22, s[44:45]
	global_load_dword v125, v23, s[44:45]
	global_load_dword v126, v24, s[44:45]
	global_load_dword v127, v25, s[44:45]
	s_add_u32 s44, s44, 0x30000
	s_addc_u32 s45, s45, 0
	global_load_dword v128, v22, s[44:45]
	global_load_dword v129, v23, s[44:45]
	global_load_dword v130, v24, s[44:45]
	global_load_dword v131, v25, s[44:45]
	s_add_u32 s44, s44, 0x30000
	s_addc_u32 s45, s45, 0
	global_load_dword v132, v22, s[44:45]
	global_load_dword v133, v23, s[44:45]
	global_load_dword v134, v24, s[44:45]
	global_load_dword v135, v25, s[44:45]
	s_add_u32 s44, s44, 0x30000
	s_addc_u32 s45, s45, 0
	global_load_dword v136, v22, s[44:45]
	global_load_dword v137, v23, s[44:45]
	global_load_dword v138, v24, s[44:45]
	global_load_dword v139, v25, s[44:45]
	s_add_u32 s44, s44, 0x30000
	s_addc_u32 s45, s45, 0
	ds_read_b128 v[68:71], v26 offset:1440
	ds_read_b128 v[76:79], v27 offset:1440
	s_waitcnt vmcnt(48)
	s_waitcnt lgkmcnt(2)
	v_mfma_f32_32x32x2_f32 v[32:47], v64, v48, v[32:47]
	v_mfma_f32_32x32x2_f32 v[32:47], v65, v49, v[32:47]
	v_mfma_f32_32x32x2_f32 v[32:47], v66, v50, v[32:47]
	v_mfma_f32_32x32x2_f32 v[32:47], v67, v51, v[32:47]
	v_fmac_f32_e32 v30, v72, v48
	v_fmac_f32_e32 v30, v73, v49
	v_fmac_f32_e32 v30, v74, v50
	v_fmac_f32_e32 v30, v75, v51
	ds_read_b128 v[64:67], v26 offset:1472
	ds_read_b128 v[72:75], v27 offset:1472
	s_waitcnt lgkmcnt(2)
	v_mfma_f32_32x32x2_f32 v[32:47], v68, v52, v[32:47]
	v_mfma_f32_32x32x2_f32 v[32:47], v69, v53, v[32:47]
	v_mfma_f32_32x32x2_f32 v[32:47], v70, v54, v[32:47]
	v_mfma_f32_32x32x2_f32 v[32:47], v71, v55, v[32:47]
	v_fmac_f32_e32 v30, v76, v52
	v_fmac_f32_e32 v30, v77, v53
	v_fmac_f32_e32 v30, v78, v54
	v_fmac_f32_e32 v30, v79, v55
	ds_read_b128 v[68:71], v26 offset:1504
	ds_read_b128 v[76:79], v27 offset:1504
	s_waitcnt lgkmcnt(2)
	v_mfma_f32_32x32x2_f32 v[32:47], v64, v56, v[32:47]
	v_mfma_f32_32x32x2_f32 v[32:47], v65, v57, v[32:47]
	v_mfma_f32_32x32x2_f32 v[32:47], v66, v58, v[32:47]
	v_mfma_f32_32x32x2_f32 v[32:47], v67, v59, v[32:47]
	v_fmac_f32_e32 v30, v72, v56
	v_fmac_f32_e32 v30, v73, v57
	v_fmac_f32_e32 v30, v74, v58
	v_fmac_f32_e32 v30, v75, v59
	ds_read_b128 v[64:67], v26 offset:1536
	ds_read_b128 v[72:75], v27 offset:1536
	s_waitcnt lgkmcnt(2)
	v_mfma_f32_32x32x2_f32 v[32:47], v68, v60, v[32:47]
	v_mfma_f32_32x32x2_f32 v[32:47], v69, v61, v[32:47]
	v_mfma_f32_32x32x2_f32 v[32:47], v70, v62, v[32:47]
	v_mfma_f32_32x32x2_f32 v[32:47], v71, v63, v[32:47]
	v_fmac_f32_e32 v30, v76, v60
	v_fmac_f32_e32 v30, v77, v61
	v_fmac_f32_e32 v30, v78, v62
	v_fmac_f32_e32 v30, v79, v63
	global_load_dword v48, v22, s[44:45]
	global_load_dword v49, v23, s[44:45]
	global_load_dword v50, v24, s[44:45]
	global_load_dword v51, v25, s[44:45]
	s_add_u32 s44, s44, 0x30000
	s_addc_u32 s45, s45, 0
	global_load_dword v52, v22, s[44:45]
	global_load_dword v53, v23, s[44:45]
	global_load_dword v54, v24, s[44:45]
	global_load_dword v55, v25, s[44:45]
	s_add_u32 s44, s44, 0x30000
	s_addc_u32 s45, s45, 0
	global_load_dword v56, v22, s[44:45]
	global_load_dword v57, v23, s[44:45]
	global_load_dword v58, v24, s[44:45]
	global_load_dword v59, v25, s[44:45]
	s_add_u32 s44, s44, 0x30000
	s_addc_u32 s45, s45, 0
	global_load_dword v60, v22, s[44:45]
	global_load_dword v61, v23, s[44:45]
	global_load_dword v62, v24, s[44:45]
	global_load_dword v63, v25, s[44:45]
	s_add_u32 s44, s44, 0x30000
	s_addc_u32 s45, s45, 0
	ds_read_b128 v[68:71], v26 offset:1568
	ds_read_b128 v[76:79], v27 offset:1568
	s_waitcnt vmcnt(48)
	s_waitcnt lgkmcnt(2)
	v_mfma_f32_32x32x2_f32 v[32:47], v64, v80, v[32:47]
	v_mfma_f32_32x32x2_f32 v[32:47], v65, v81, v[32:47]
	v_mfma_f32_32x32x2_f32 v[32:47], v66, v82, v[32:47]
	v_mfma_f32_32x32x2_f32 v[32:47], v67, v83, v[32:47]
	v_fmac_f32_e32 v30, v72, v80
	v_fmac_f32_e32 v30, v73, v81
	v_fmac_f32_e32 v30, v74, v82
	v_fmac_f32_e32 v30, v75, v83
	ds_read_b128 v[64:67], v26 offset:1600
	ds_read_b128 v[72:75], v27 offset:1600
	s_waitcnt lgkmcnt(2)
	v_mfma_f32_32x32x2_f32 v[32:47], v68, v84, v[32:47]
	v_mfma_f32_32x32x2_f32 v[32:47], v69, v85, v[32:47]
	v_mfma_f32_32x32x2_f32 v[32:47], v70, v86, v[32:47]
	v_mfma_f32_32x32x2_f32 v[32:47], v71, v87, v[32:47]
	v_fmac_f32_e32 v30, v76, v84
	v_fmac_f32_e32 v30, v77, v85
	v_fmac_f32_e32 v30, v78, v86
	v_fmac_f32_e32 v30, v79, v87
	ds_read_b128 v[68:71], v26 offset:1632
	ds_read_b128 v[76:79], v27 offset:1632
	s_waitcnt lgkmcnt(2)
	v_mfma_f32_32x32x2_f32 v[32:47], v64, v88, v[32:47]
	v_mfma_f32_32x32x2_f32 v[32:47], v65, v89, v[32:47]
	v_mfma_f32_32x32x2_f32 v[32:47], v66, v90, v[32:47]
	v_mfma_f32_32x32x2_f32 v[32:47], v67, v91, v[32:47]
	v_fmac_f32_e32 v30, v72, v88
	v_fmac_f32_e32 v30, v73, v89
	v_fmac_f32_e32 v30, v74, v90
	v_fmac_f32_e32 v30, v75, v91
	ds_read_b128 v[64:67], v26 offset:1664
	ds_read_b128 v[72:75], v27 offset:1664
	s_waitcnt lgkmcnt(2)
	v_mfma_f32_32x32x2_f32 v[32:47], v68, v92, v[32:47]
	v_mfma_f32_32x32x2_f32 v[32:47], v69, v93, v[32:47]
	v_mfma_f32_32x32x2_f32 v[32:47], v70, v94, v[32:47]
	v_mfma_f32_32x32x2_f32 v[32:47], v71, v95, v[32:47]
	v_fmac_f32_e32 v30, v76, v92
	v_fmac_f32_e32 v30, v77, v93
	v_fmac_f32_e32 v30, v78, v94
	v_fmac_f32_e32 v30, v79, v95
	ds_read_b128 v[68:71], v26 offset:1696
	ds_read_b128 v[76:79], v27 offset:1696
	s_waitcnt vmcnt(32)
	s_waitcnt lgkmcnt(2)
	v_mfma_f32_32x32x2_f32 v[32:47], v64, v108, v[32:47]
	v_mfma_f32_32x32x2_f32 v[32:47], v65, v109, v[32:47]
	v_mfma_f32_32x32x2_f32 v[32:47], v66, v110, v[32:47]
	v_mfma_f32_32x32x2_f32 v[32:47], v67, v111, v[32:47]
	v_fmac_f32_e32 v30, v72, v108
	v_fmac_f32_e32 v30, v73, v109
	v_fmac_f32_e32 v30, v74, v110
	v_fmac_f32_e32 v30, v75, v111
	ds_read_b128 v[64:67], v26 offset:1728
	ds_read_b128 v[72:75], v27 offset:1728
	s_waitcnt lgkmcnt(2)
	v_mfma_f32_32x32x2_f32 v[32:47], v68, v112, v[32:47]
	v_mfma_f32_32x32x2_f32 v[32:47], v69, v113, v[32:47]
	v_mfma_f32_32x32x2_f32 v[32:47], v70, v114, v[32:47]
	v_mfma_f32_32x32x2_f32 v[32:47], v71, v115, v[32:47]
	v_fmac_f32_e32 v30, v76, v112
	v_fmac_f32_e32 v30, v77, v113
	v_fmac_f32_e32 v30, v78, v114
	v_fmac_f32_e32 v30, v79, v115
	ds_read_b128 v[68:71], v26 offset:1760
	ds_read_b128 v[76:79], v27 offset:1760
	s_waitcnt lgkmcnt(2)
	v_mfma_f32_32x32x2_f32 v[32:47], v64, v116, v[32:47]
	v_mfma_f32_32x32x2_f32 v[32:47], v65, v117, v[32:47]
	v_mfma_f32_32x32x2_f32 v[32:47], v66, v118, v[32:47]
	v_mfma_f32_32x32x2_f32 v[32:47], v67, v119, v[32:47]
	v_fmac_f32_e32 v30, v72, v116
	v_fmac_f32_e32 v30, v73, v117
	v_fmac_f32_e32 v30, v74, v118
	v_fmac_f32_e32 v30, v75, v119
	ds_read_b128 v[64:67], v26 offset:1792
	ds_read_b128 v[72:75], v27 offset:1792
	s_waitcnt lgkmcnt(2)
	v_mfma_f32_32x32x2_f32 v[32:47], v68, v120, v[32:47]
	v_mfma_f32_32x32x2_f32 v[32:47], v69, v121, v[32:47]
	v_mfma_f32_32x32x2_f32 v[32:47], v70, v122, v[32:47]
	v_mfma_f32_32x32x2_f32 v[32:47], v71, v123, v[32:47]
	v_fmac_f32_e32 v30, v76, v120
	v_fmac_f32_e32 v30, v77, v121
	v_fmac_f32_e32 v30, v78, v122
	v_fmac_f32_e32 v30, v79, v123
	ds_read_b128 v[68:71], v26 offset:1824
	ds_read_b128 v[76:79], v27 offset:1824
	s_waitcnt vmcnt(16)
	s_waitcnt lgkmcnt(2)
	v_mfma_f32_32x32x2_f32 v[32:47], v64, v124, v[32:47]
	v_mfma_f32_32x32x2_f32 v[32:47], v65, v125, v[32:47]
	v_mfma_f32_32x32x2_f32 v[32:47], v66, v126, v[32:47]
	v_mfma_f32_32x32x2_f32 v[32:47], v67, v127, v[32:47]
	v_fmac_f32_e32 v30, v72, v124
	v_fmac_f32_e32 v30, v73, v125
	v_fmac_f32_e32 v30, v74, v126
	v_fmac_f32_e32 v30, v75, v127
	ds_read_b128 v[64:67], v26 offset:1856
	ds_read_b128 v[72:75], v27 offset:1856
	s_waitcnt lgkmcnt(2)
	v_mfma_f32_32x32x2_f32 v[32:47], v68, v128, v[32:47]
	v_mfma_f32_32x32x2_f32 v[32:47], v69, v129, v[32:47]
	v_mfma_f32_32x32x2_f32 v[32:47], v70, v130, v[32:47]
	v_mfma_f32_32x32x2_f32 v[32:47], v71, v131, v[32:47]
	v_fmac_f32_e32 v30, v76, v128
	v_fmac_f32_e32 v30, v77, v129
	v_fmac_f32_e32 v30, v78, v130
	v_fmac_f32_e32 v30, v79, v131
	ds_read_b128 v[68:71], v26 offset:1888
	ds_read_b128 v[76:79], v27 offset:1888
	s_waitcnt lgkmcnt(2)
	v_mfma_f32_32x32x2_f32 v[32:47], v64, v132, v[32:47]
	v_mfma_f32_32x32x2_f32 v[32:47], v65, v133, v[32:47]
	v_mfma_f32_32x32x2_f32 v[32:47], v66, v134, v[32:47]
	v_mfma_f32_32x32x2_f32 v[32:47], v67, v135, v[32:47]
	v_fmac_f32_e32 v30, v72, v132
	v_fmac_f32_e32 v30, v73, v133
	v_fmac_f32_e32 v30, v74, v134
	v_fmac_f32_e32 v30, v75, v135
	ds_read_b128 v[64:67], v26 offset:1920
	ds_read_b128 v[72:75], v27 offset:1920
	s_waitcnt lgkmcnt(2)
	v_mfma_f32_32x32x2_f32 v[32:47], v68, v136, v[32:47]
	v_mfma_f32_32x32x2_f32 v[32:47], v69, v137, v[32:47]
	v_mfma_f32_32x32x2_f32 v[32:47], v70, v138, v[32:47]
	v_mfma_f32_32x32x2_f32 v[32:47], v71, v139, v[32:47]
	v_fmac_f32_e32 v30, v76, v136
	v_fmac_f32_e32 v30, v77, v137
	v_fmac_f32_e32 v30, v78, v138
	v_fmac_f32_e32 v30, v79, v139
	ds_read_b128 v[68:71], v26 offset:1952
	ds_read_b128 v[76:79], v27 offset:1952
	s_waitcnt vmcnt(0)
	s_waitcnt lgkmcnt(2)
	v_mfma_f32_32x32x2_f32 v[32:47], v64, v48, v[32:47]
	v_mfma_f32_32x32x2_f32 v[32:47], v65, v49, v[32:47]
	v_mfma_f32_32x32x2_f32 v[32:47], v66, v50, v[32:47]
	v_mfma_f32_32x32x2_f32 v[32:47], v67, v51, v[32:47]
	v_fmac_f32_e32 v30, v72, v48
	v_fmac_f32_e32 v30, v73, v49
	v_fmac_f32_e32 v30, v74, v50
	v_fmac_f32_e32 v30, v75, v51
	ds_read_b128 v[64:67], v26 offset:1984
	ds_read_b128 v[72:75], v27 offset:1984
	s_waitcnt lgkmcnt(2)
	v_mfma_f32_32x32x2_f32 v[32:47], v68, v52, v[32:47]
	v_mfma_f32_32x32x2_f32 v[32:47], v69, v53, v[32:47]
	v_mfma_f32_32x32x2_f32 v[32:47], v70, v54, v[32:47]
	v_mfma_f32_32x32x2_f32 v[32:47], v71, v55, v[32:47]
	v_fmac_f32_e32 v30, v76, v52
	v_fmac_f32_e32 v30, v77, v53
	v_fmac_f32_e32 v30, v78, v54
	v_fmac_f32_e32 v30, v79, v55
	ds_read_b128 v[68:71], v26 offset:2016
	ds_read_b128 v[76:79], v27 offset:2016
	s_waitcnt lgkmcnt(2)
	v_mfma_f32_32x32x2_f32 v[32:47], v64, v56, v[32:47]
	v_mfma_f32_32x32x2_f32 v[32:47], v65, v57, v[32:47]
	v_mfma_f32_32x32x2_f32 v[32:47], v66, v58, v[32:47]
	v_mfma_f32_32x32x2_f32 v[32:47], v67, v59, v[32:47]
	v_fmac_f32_e32 v30, v72, v56
	v_fmac_f32_e32 v30, v73, v57
	v_fmac_f32_e32 v30, v74, v58
	v_fmac_f32_e32 v30, v75, v59
	s_waitcnt lgkmcnt(0)
	v_mfma_f32_32x32x2_f32 v[32:47], v68, v60, v[32:47]
	v_mfma_f32_32x32x2_f32 v[32:47], v69, v61, v[32:47]
	v_mfma_f32_32x32x2_f32 v[32:47], v70, v62, v[32:47]
	v_mfma_f32_32x32x2_f32 v[32:47], v71, v63, v[32:47]
	v_fmac_f32_e32 v30, v76, v60
	v_fmac_f32_e32 v30, v77, v61
	v_fmac_f32_e32 v30, v78, v62
	v_fmac_f32_e32 v30, v79, v63
	s_nop 15
	s_nop 7
	s_barrier
	s_mul_i32 s52, s50, 0x4200
	s_lshl_b32 s53, s49, 7
	s_add_i32 s52, s52, s53
	v_lshlrev_b32_e32 v28, 11, v21
	v_lshl_add_u32 v28, v20, 2, v28
	v_add_u32_e32 v28, s52, v28
	ds_write_b32 v28, v32 offset:0
	ds_write_b32 v28, v33 offset:512
	ds_write_b32 v28, v34 offset:1024
	ds_write_b32 v28, v35 offset:1536
	ds_write_b32 v28, v36 offset:4096
	ds_write_b32 v28, v37 offset:4608
	ds_write_b32 v28, v38 offset:5120
	ds_write_b32 v28, v39 offset:5632
	ds_write_b32 v28, v40 offset:8192
	ds_write_b32 v28, v41 offset:8704
	ds_write_b32 v28, v42 offset:9216
	ds_write_b32 v28, v43 offset:9728
	ds_write_b32 v28, v44 offset:12288
	ds_write_b32 v28, v45 offset:12800
	ds_write_b32 v28, v46 offset:13312
	ds_write_b32 v28, v47 offset:13824
	s_lshl_b32 s52, s50, 10
	s_add_i32 s52, s52, s53
	s_add_i32 s52, s52, 0x8400
	v_lshlrev_b32_e32 v29, 9, v21
	v_lshl_add_u32 v29, v20, 2, v29
	v_add_u32_e32 v29, s52, v29
	ds_write_b32 v29, v30
	s_waitcnt lgkmcnt(0)
	s_barrier
	s_mul_i32 s52, s42, 0x6000
	s_lshl_b32 s53, s43, 2
	s_add_i32 s54, s52, s53
	s_add_u32 s46, s46, s54
	s_addc_u32 s47, s47, 0
	s_mul_i32 s52, s42, 0xc6000
	s_add_i32 s52, s52, s53
	s_add_u32 s54, s18, s52
	s_addc_u32 s55, s19, 0
	v_add_u32_e32 v18, 0, v2
	v_lshlrev_b32_e32 v19, 2, v18
	ds_read_b32 v20, v19
	ds_read_b32 v21, v19 offset:16896
	v_and_b32_e32 v22, 0x7f, v18
	v_lshlrev_b32_e32 v22, 2, v22
	global_load_dword v23, v22, s[46:47]
	v_lshrrev_b32_e32 v24, 7, v18
	v_mul_u32_u24_e32 v24, 0x6000, v24
	v_add_u32_e32 v24, v24, v22
	s_waitcnt lgkmcnt(0)
	v_add_f32_e32 v20, v20, v21
	s_waitcnt vmcnt(0)
	v_add_f32_e32 v20, v20, v23
	global_store_dword v24, v20, s[54:55]
	v_add_u32_e32 v18, 512, v2
	v_lshlrev_b32_e32 v19, 2, v18
	ds_read_b32 v20, v19
	ds_read_b32 v21, v19 offset:16896
	v_and_b32_e32 v22, 0x7f, v18
	v_lshlrev_b32_e32 v22, 2, v22
	global_load_dword v23, v22, s[46:47]
	v_lshrrev_b32_e32 v24, 7, v18
	v_mul_u32_u24_e32 v24, 0x6000, v24
	v_add_u32_e32 v24, v24, v22
	s_waitcnt lgkmcnt(0)
	v_add_f32_e32 v20, v20, v21
	s_waitcnt vmcnt(0)
	v_add_f32_e32 v20, v20, v23
	global_store_dword v24, v20, s[54:55]
	v_add_u32_e32 v18, 1024, v2
	v_lshlrev_b32_e32 v19, 2, v18
	ds_read_b32 v20, v19
	ds_read_b32 v21, v19 offset:16896
	v_and_b32_e32 v22, 0x7f, v18
	v_lshlrev_b32_e32 v22, 2, v22
	global_load_dword v23, v22, s[46:47]
	v_lshrrev_b32_e32 v24, 7, v18
	v_mul_u32_u24_e32 v24, 0x6000, v24
	v_add_u32_e32 v24, v24, v22
	s_waitcnt lgkmcnt(0)
	v_add_f32_e32 v20, v20, v21
	s_waitcnt vmcnt(0)
	v_add_f32_e32 v20, v20, v23
	global_store_dword v24, v20, s[54:55]
	v_add_u32_e32 v18, 1536, v2
	v_lshlrev_b32_e32 v19, 2, v18
	ds_read_b32 v20, v19
	ds_read_b32 v21, v19 offset:16896
	v_and_b32_e32 v22, 0x7f, v18
	v_lshlrev_b32_e32 v22, 2, v22
	global_load_dword v23, v22, s[46:47]
	v_lshrrev_b32_e32 v24, 7, v18
	v_mul_u32_u24_e32 v24, 0x6000, v24
	v_add_u32_e32 v24, v24, v22
	s_waitcnt lgkmcnt(0)
	v_add_f32_e32 v20, v20, v21
	s_waitcnt vmcnt(0)
	v_add_f32_e32 v20, v20, v23
	global_store_dword v24, v20, s[54:55]
	v_add_u32_e32 v18, 2048, v2
	v_lshlrev_b32_e32 v19, 2, v18
	ds_read_b32 v20, v19
	ds_read_b32 v21, v19 offset:16896
	v_and_b32_e32 v22, 0x7f, v18
	v_lshlrev_b32_e32 v22, 2, v22
	global_load_dword v23, v22, s[46:47]
	v_lshrrev_b32_e32 v24, 7, v18
	v_mul_u32_u24_e32 v24, 0x6000, v24
	v_add_u32_e32 v24, v24, v22
	s_waitcnt lgkmcnt(0)
	v_add_f32_e32 v20, v20, v21
	s_waitcnt vmcnt(0)
	v_add_f32_e32 v20, v20, v23
	global_store_dword v24, v20, s[54:55]
	v_add_u32_e32 v18, 2560, v2
	v_lshlrev_b32_e32 v19, 2, v18
	ds_read_b32 v20, v19
	ds_read_b32 v21, v19 offset:16896
	v_and_b32_e32 v22, 0x7f, v18
	v_lshlrev_b32_e32 v22, 2, v22
	global_load_dword v23, v22, s[46:47]
	v_lshrrev_b32_e32 v24, 7, v18
	v_mul_u32_u24_e32 v24, 0x6000, v24
	v_add_u32_e32 v24, v24, v22
	s_waitcnt lgkmcnt(0)
	v_add_f32_e32 v20, v20, v21
	s_waitcnt vmcnt(0)
	v_add_f32_e32 v20, v20, v23
	global_store_dword v24, v20, s[54:55]
	v_add_u32_e32 v18, 3072, v2
	v_lshlrev_b32_e32 v19, 2, v18
	ds_read_b32 v20, v19
	ds_read_b32 v21, v19 offset:16896
	v_and_b32_e32 v22, 0x7f, v18
	v_lshlrev_b32_e32 v22, 2, v22
	global_load_dword v23, v22, s[46:47]
	v_lshrrev_b32_e32 v24, 7, v18
	v_mul_u32_u24_e32 v24, 0x6000, v24
	v_add_u32_e32 v24, v24, v22
	s_waitcnt lgkmcnt(0)
	v_add_f32_e32 v20, v20, v21
	s_waitcnt vmcnt(0)
	v_add_f32_e32 v20, v20, v23
	global_store_dword v24, v20, s[54:55]
	v_add_u32_e32 v18, 3584, v2
	v_lshlrev_b32_e32 v19, 2, v18
	ds_read_b32 v20, v19
	ds_read_b32 v21, v19 offset:16896
	v_and_b32_e32 v22, 0x7f, v18
	v_lshlrev_b32_e32 v22, 2, v22
	global_load_dword v23, v22, s[46:47]
	v_lshrrev_b32_e32 v24, 7, v18
	v_mul_u32_u24_e32 v24, 0x6000, v24
	v_add_u32_e32 v24, v24, v22
	s_waitcnt lgkmcnt(0)
	v_add_f32_e32 v20, v20, v21
	s_waitcnt vmcnt(0)
	v_add_f32_e32 v20, v20, v23
	global_store_dword v24, v20, s[54:55]
	v_cmp_gt_u32_e32 vcc, 0x80, v2
	s_and_saveexec_b64 s[56:57], vcc
	s_cbranch_execz .Lmod_r32_done
	v_lshlrev_b32_e32 v19, 2, v2
	ds_read_b32 v20, v19 offset:33792
	ds_read_b32 v21, v19 offset:34304
	ds_read_b32 v22, v19 offset:34816
	ds_read_b32 v23, v19 offset:35328
	global_load_dword v25, v19, s[46:47]
	s_waitcnt lgkmcnt(0)
	v_add_f32_e32 v20, v20, v21
	v_add_f32_e32 v22, v22, v23
	v_add_f32_e32 v20, v20, v22
	s_waitcnt vmcnt(0)
	v_add_f32_e32 v20, v20, v25
	v_add_u32_e32 v24, 0xc0000, v19
	global_store_dword v24, v20, s[54:55]
.Lmod_r32_done:
	s_or_b64 exec, exec, s[56:57]
	s_branch .LBB0_60
